# speedup vs baseline: 1.0132x; 1.0074x over previous
.LBB2_5:
	ds_read_b128 v[102:105], v120 offset:8192
	ds_read_b128 v[106:109], v120 offset:10240
	v_exp_f32_e32 v69, v46
	v_exp_f32_e32 v71, v47
	v_exp_f32_e32 v73, v48
	v_exp_f32_e32 v75, v49
	ds_read_b128 v[110:113], v120 offset:12288
	ds_read_b128 v[46:49], v120 offset:14336
	v_exp_f32_e32 v42, v42
	v_exp_f32_e32 v43, v43
	v_exp_f32_e32 v44, v44
	v_exp_f32_e32 v45, v45
	v_cvt_pk_f16_f32 v76, v69, v71
	v_cvt_pk_f16_f32 v77, v73, v75
	v_cvt_pk_f16_f32 v78, v42, v43
	v_cvt_pk_f16_f32 v79, v44, v45
	ds_read_b128 v[42:45], v121 offset:8192
	v_exp_f32_e32 v38, v38
	v_exp_f32_e32 v39, v39
	s_waitcnt lgkmcnt(4)
	v_mfma_f32_16x16x32_f16 v[26:29], v[102:105], v[76:79], v[26:29]
	v_exp_f32_e32 v40, v40
	v_exp_f32_e32 v41, v41
	s_waitcnt lgkmcnt(3)
	v_mfma_f32_16x16x32_f16 v[22:25], v[106:109], v[76:79], v[22:25]
	ds_read_b128 v[102:105], v121 offset:10240
	v_exp_f32_e32 v34, v34
	v_exp_f32_e32 v35, v35
	s_waitcnt lgkmcnt(3)
	v_mfma_f32_16x16x32_f16 v[18:21], v[110:113], v[76:79], v[18:21]
	ds_read_b128 v[106:109], v121 offset:12288
	v_exp_f32_e32 v36, v36
	v_exp_f32_e32 v37, v37
	s_waitcnt lgkmcnt(3)
	v_mfma_f32_16x16x32_f16 v[10:13], v[46:49], v[76:79], v[10:13]
	ds_read_b128 v[110:113], v121 offset:14336
	v_mfma_f32_16x16x32_f16 v[14:17], v[116:119], v[76:79], v[14:17]
	v_cvt_pk_f16_f32 v37, v36, v37
	v_cvt_pk_f16_f32 v36, v34, v35
	v_cvt_pk_f16_f32 v35, v40, v41
	v_cvt_pk_f16_f32 v34, v38, v39
	s_mov_b64 s[38:39], 0
	s_waitcnt lgkmcnt(3)
	v_mfma_f32_16x16x32_f16 v[26:29], v[42:45], v[34:37], v[26:29]
	s_waitcnt lgkmcnt(2)
	v_mfma_f32_16x16x32_f16 v[22:25], v[102:105], v[34:37], v[22:25]
	s_waitcnt lgkmcnt(1)
	v_mfma_f32_16x16x32_f16 v[18:21], v[106:109], v[34:37], v[18:21]
	s_waitcnt lgkmcnt(0)
	v_mfma_f32_16x16x32_f16 v[10:13], v[110:113], v[34:37], v[10:13]
	v_mfma_f32_16x16x32_f16 v[14:17], v[116:119], v[34:37], v[14:17]
	s_cmp_eq_u32 s55, 0
	s_cbranch_scc1 .LBB2_6
	s_mov_b32 s80, 0
	s_cmp_eq_u32 s81, 0
	s_cbranch_scc1 .Lattn_A
	s_branch .Lattn_post
